# P1 epilogue RoPE tiles: cos/sin table rows prefetched two pairs ahead into free fragment registers, in-epilogue vmcnt(0)/store waits removed
# speedup vs baseline: 1.0044x; 1.0004x over previous
.LBB0_189:
	s_cmp_lt_i32 s28, 64
	v_lshl_add_u32 v18, s6, 8, v188
	s_cselect_b64 s[6:7], -1, 0
	s_lshl_b64 s[30:31], 1, s28
	s_and_b32 s9, s31, 0x333ff
	s_cmp_lg_u64 s[8:9], 0
	s_cselect_b64 s[30:31], -1, 0
	s_and_b64 s[30:31], s[16:17], s[30:31]
	s_and_b64 s[30:31], s[6:7], s[30:31]
	v_cndmask_b32_e64 v0, 0, 1, s[30:31]
	v_cmp_ne_u32_e64 s[6:7], 1, v0
	s_andn2_b64 vcc, exec, s[30:31]
	v_ashrrev_i32_e32 v19, 31, v18
	s_cbranch_vccnz .LBB0_191
	s_nop 1
	v_mov_b32_e32 v196, v18
	v_ashrrev_i32_e32 v197, 31, v196
	v_lshlrev_b64 v[196:197], 6, v[196:197]
	v_lshl_add_u64 v[200:201], v[172:173], 0, v[196:197]
	v_lshl_add_u64 v[204:205], v[174:175], 0, v[196:197]
	global_load_dwordx4 v[196:199], v[200:201], off offset:16
	global_load_dwordx4 v[208:211], v[200:201], off
	global_load_dwordx4 v[200:203], v[204:205], off
	s_nop 0
	global_load_dwordx4 v[204:207], v[204:205], off offset:16
	v_add_u32_e32 v212, 16, v18
	v_ashrrev_i32_e32 v213, 31, v212
	v_lshlrev_b64 v[212:213], 6, v[212:213]
	v_lshl_add_u64 v[216:217], v[172:173], 0, v[212:213]
	v_lshl_add_u64 v[220:221], v[174:175], 0, v[212:213]
	global_load_dwordx4 v[212:215], v[216:217], off offset:16
	global_load_dwordx4 v[224:227], v[216:217], off
	global_load_dwordx4 v[216:219], v[220:221], off
	s_nop 0
	global_load_dwordx4 v[220:223], v[220:221], off offset:16
	s_waitcnt vmcnt(4)
	v_mov_b64_e32 v[2:3], v[196:197]
	v_mov_b64_e32 v[4:5], v[198:199]
	v_mov_b64_e32 v[14:15], v[208:209]
	v_mov_b64_e32 v[16:17], v[210:211]
	v_mov_b64_e32 v[10:11], v[200:201]
	v_mov_b64_e32 v[12:13], v[202:203]
	v_mov_b64_e32 v[6:7], v[204:205]
	v_mov_b64_e32 v[8:9], v[206:207]
	v_add_u32_e32 v196, 32, v18
	v_ashrrev_i32_e32 v197, 31, v196
	v_lshlrev_b64 v[196:197], 6, v[196:197]
	v_lshl_add_u64 v[200:201], v[172:173], 0, v[196:197]
	v_lshl_add_u64 v[204:205], v[174:175], 0, v[196:197]
	global_load_dwordx4 v[196:199], v[200:201], off offset:16
	global_load_dwordx4 v[208:211], v[200:201], off
	global_load_dwordx4 v[200:203], v[204:205], off
	s_nop 0
	global_load_dwordx4 v[204:207], v[204:205], off offset:16
	s_branch .LBB0_192
.LBB0_191:
.LBB0_192:
	v_pk_mul_f32 v[22:23], v[160:161], s[18:19] op_sel_hi:[1,0]
	v_pk_mul_f32 v[26:27], v[158:159], s[18:19] op_sel_hi:[1,0]
	v_pk_mul_f32 v[24:25], v[156:157], s[18:19] op_sel_hi:[1,0]
	s_and_b64 vcc, exec, s[6:7]
	v_pk_mul_f32 v[28:29], v[154:155], s[18:19] op_sel_hi:[1,0]
	s_cbranch_vccnz .LBB0_194
	v_and_b32_e32 v19, 64, v195
	v_xor_b32_e32 v0, 32, v195
	v_add_u32_e32 v19, 64, v19
	v_cmp_lt_i32_e32 vcc, v0, v19
	v_mov_b32_e32 v158, v23
	v_mov_b32_e32 v159, v13
	v_cndmask_b32_e32 v0, v195, v0, vcc
	v_lshlrev_b32_e32 v0, 2, v0
	ds_bpermute_b32 v19, v0, v22
	ds_bpermute_b32 v33, v0, v24
	ds_bpermute_b32 v20, v0, v26
	ds_bpermute_b32 v21, v0, v27
	ds_bpermute_b32 v30, v0, v28
	s_waitcnt lgkmcnt(4)
	v_mul_f32_e32 v19, v170, v19
	v_mul_f32_e32 v32, v12, v19
	ds_bpermute_b32 v19, v0, v23
	ds_bpermute_b32 v31, v0, v29
	ds_bpermute_b32 v0, v0, v25
	v_mov_b32_e32 v156, v17
	s_waitcnt lgkmcnt(6)
	v_mul_f32_e32 v33, v170, v33
	s_waitcnt lgkmcnt(2)
	v_mul_f32_e32 v157, v170, v19
	v_pk_mul_f32 v[156:157], v[158:159], v[156:157]
	v_pk_mul_f32 v[26:27], v[26:27], v[14:15]
	v_pk_mul_f32 v[20:21], v[170:171], v[20:21]
	v_mul_f32_e32 v22, v22, v16
	v_mul_f32_e32 v154, v8, v33
	v_mov_b32_e32 v23, v156
	v_mov_b32_e32 v33, v157
	v_pk_fma_f32 v[26:27], v[10:11], v[20:21], v[26:27]
	v_pk_add_f32 v[22:23], v[22:23], v[32:33]
	s_waitcnt lgkmcnt(0)
	v_mul_f32_e32 v21, v170, v0
	v_mov_b32_e32 v32, v25
	v_mov_b32_e32 v33, v9
	v_mov_b32_e32 v20, v5
	v_pk_mul_f32 v[20:21], v[32:33], v[20:21]
	v_pk_mul_f32 v[28:29], v[28:29], v[2:3]
	v_pk_mul_f32 v[30:31], v[170:171], v[30:31]
	v_mul_f32_e32 v24, v24, v4
	v_mov_b32_e32 v25, v20
	v_mov_b32_e32 v155, v21
	v_pk_fma_f32 v[28:29], v[6:7], v[30:31], v[28:29]
	v_pk_add_f32 v[24:25], v[24:25], v[154:155]
.LBB0_194:
	v_lshl_or_b32 v20, s28, 8, v190
	v_cvt_pk_bf16_f32 v26, v26, v27
	v_cvt_pk_bf16_f32 v27, v22, v23
	v_mov_b64_e32 v[22:23], s[96:97]
	v_ashrrev_i32_e32 v21, 31, v20
	v_mad_i64_i32 v[22:23], s[30:31], v18, s51, v[22:23]
	v_cvt_pk_bf16_f32 v28, v28, v29
	v_cvt_pk_bf16_f32 v29, v24, v25
	v_lshl_add_u64 v[22:23], v[20:21], 1, v[22:23]
	global_store_dwordx4 v[22:23], v[26:29], off nt
	v_pk_mul_f32 v[24:25], v[152:153], s[18:19] op_sel_hi:[1,0]
	s_and_b64 vcc, exec, s[6:7]
	v_pk_mul_f32 v[28:29], v[150:151], s[18:19] op_sel_hi:[1,0]
	v_pk_mul_f32 v[26:27], v[148:149], s[18:19] op_sel_hi:[1,0]
	v_pk_mul_f32 v[30:31], v[146:147], s[18:19] op_sel_hi:[1,0]
	s_cbranch_vccnz .LBB0_196
	v_and_b32_e32 v19, 64, v195
	v_xor_b32_e32 v0, 32, v195
	v_add_u32_e32 v19, 64, v19
	v_cmp_lt_i32_e32 vcc, v0, v19
	v_pk_mul_f32 v[14:15], v[28:29], v[14:15]
	v_mul_f32_e32 v16, v24, v16
	v_cndmask_b32_e32 v0, v195, v0, vcc
	v_lshlrev_b32_e32 v0, 2, v0
	ds_bpermute_b32 v32, v0, v28
	ds_bpermute_b32 v33, v0, v29
	ds_bpermute_b32 v19, v0, v24
	ds_bpermute_b32 v146, v0, v30
	ds_bpermute_b32 v147, v0, v31
	v_mul_f32_e32 v4, v26, v4
	s_waitcnt lgkmcnt(3)
	v_pk_mul_f32 v[28:29], v[170:171], v[32:33]
	ds_bpermute_b32 v32, v0, v26
	s_waitcnt lgkmcnt(3)
	v_mul_f32_e32 v19, v170, v19
	v_mul_f32_e32 v24, v12, v19
	ds_bpermute_b32 v12, v0, v25
	ds_bpermute_b32 v0, v0, v27
	s_waitcnt lgkmcnt(2)
	v_mul_f32_e32 v19, v170, v32
	v_mul_f32_e32 v26, v8, v19
	v_mov_b32_e32 v32, v17
	s_waitcnt lgkmcnt(1)
	v_mul_f32_e32 v33, v170, v12
	v_mov_b32_e32 v12, v25
	v_pk_fma_f32 v[28:29], v[10:11], v[28:29], v[14:15]
	s_waitcnt lgkmcnt(0)
	v_mul_f32_e32 v11, v170, v0
	v_mov_b32_e32 v8, v27
	v_mov_b32_e32 v10, v5
	v_pk_mul_f32 v[12:13], v[12:13], v[32:33]
	v_pk_mul_f32 v[8:9], v[8:9], v[10:11]
	v_pk_mul_f32 v[2:3], v[30:31], v[2:3]
	v_pk_mul_f32 v[30:31], v[170:171], v[146:147]
	v_mov_b32_e32 v17, v12
	v_mov_b32_e32 v25, v13
	v_mov_b32_e32 v5, v8
	v_mov_b32_e32 v27, v9
	v_pk_add_f32 v[24:25], v[16:17], v[24:25]
	v_pk_fma_f32 v[30:31], v[6:7], v[30:31], v[2:3]
	v_pk_add_f32 v[26:27], v[4:5], v[26:27]
.LBB0_196:
	v_cvt_pk_bf16_f32 v2, v28, v29
	v_cvt_pk_bf16_f32 v3, v24, v25
	v_cvt_pk_bf16_f32 v4, v30, v31
	v_cvt_pk_bf16_f32 v5, v26, v27
	global_store_dwordx4 v[22:23], v[2:5], off offset:256 nt
	v_or_b32_e32 v22, 16, v18
	s_and_b64 vcc, exec, s[6:7]
	v_ashrrev_i32_e32 v23, 31, v22
	s_cbranch_vccnz .LBB0_198
	s_nop 1
	s_waitcnt vmcnt(6)
	v_mov_b64_e32 v[2:3], v[212:213]
	v_mov_b64_e32 v[4:5], v[214:215]
	v_mov_b64_e32 v[14:15], v[224:225]
	v_mov_b64_e32 v[16:17], v[226:227]
	v_mov_b64_e32 v[10:11], v[216:217]
	v_mov_b64_e32 v[12:13], v[218:219]
	v_mov_b64_e32 v[6:7], v[220:221]
	v_mov_b64_e32 v[8:9], v[222:223]
	v_add_u32_e32 v212, 48, v18
	v_ashrrev_i32_e32 v213, 31, v212
	v_lshlrev_b64 v[212:213], 6, v[212:213]
	v_lshl_add_u64 v[216:217], v[172:173], 0, v[212:213]
	v_lshl_add_u64 v[220:221], v[174:175], 0, v[212:213]
	global_load_dwordx4 v[212:215], v[216:217], off offset:16
	global_load_dwordx4 v[224:227], v[216:217], off
	global_load_dwordx4 v[216:219], v[220:221], off
	s_nop 0
	global_load_dwordx4 v[220:223], v[220:221], off offset:16
	s_branch .LBB0_199
.LBB0_198:
.LBB0_199:
	v_pk_mul_f32 v[24:25], v[144:145], s[18:19] op_sel_hi:[1,0]
	v_pk_mul_f32 v[28:29], v[142:143], s[18:19] op_sel_hi:[1,0]
	v_pk_mul_f32 v[26:27], v[140:141], s[18:19] op_sel_hi:[1,0]
	s_and_b64 vcc, exec, s[6:7]
	v_pk_mul_f32 v[30:31], v[138:139], s[18:19] op_sel_hi:[1,0]
	s_cbranch_vccnz .LBB0_201
	v_and_b32_e32 v19, 64, v195
	v_xor_b32_e32 v0, 32, v195
	v_add_u32_e32 v19, 64, v19
	v_cmp_lt_i32_e32 vcc, v0, v19
	v_mov_b32_e32 v146, v25
	v_mov_b32_e32 v147, v13
	v_cndmask_b32_e32 v0, v195, v0, vcc
	v_lshlrev_b32_e32 v0, 2, v0
	ds_bpermute_b32 v19, v0, v24
	ds_bpermute_b32 v32, v0, v28
	ds_bpermute_b32 v33, v0, v29
	ds_bpermute_b32 v138, v0, v30
	ds_bpermute_b32 v139, v0, v31
	s_waitcnt lgkmcnt(4)
	v_mul_f32_e32 v19, v170, v19
	v_mul_f32_e32 v140, v12, v19
	ds_bpermute_b32 v19, v0, v25
	ds_bpermute_b32 v23, v0, v26
	ds_bpermute_b32 v0, v0, v27
	v_mov_b32_e32 v144, v17
	v_pk_mul_f32 v[28:29], v[28:29], v[14:15]
	s_waitcnt lgkmcnt(2)
	v_mul_f32_e32 v145, v170, v19
	v_pk_mul_f32 v[144:145], v[146:147], v[144:145]
	v_pk_mul_f32 v[32:33], v[170:171], v[32:33]
	v_mul_f32_e32 v24, v24, v16
	v_mov_b32_e32 v25, v144
	v_mov_b32_e32 v141, v145
	v_pk_fma_f32 v[28:29], v[10:11], v[32:33], v[28:29]
	v_pk_add_f32 v[24:25], v[24:25], v[140:141]
	s_waitcnt lgkmcnt(0)
	v_mul_f32_e32 v33, v170, v0
	v_mov_b32_e32 v140, v27
	v_mov_b32_e32 v141, v9
	v_mov_b32_e32 v32, v5
	v_mul_f32_e32 v23, v170, v23
	v_pk_mul_f32 v[32:33], v[140:141], v[32:33]
	v_pk_mul_f32 v[30:31], v[30:31], v[2:3]
	v_pk_mul_f32 v[138:139], v[170:171], v[138:139]
	v_mul_f32_e32 v26, v26, v4
	v_mul_f32_e32 v142, v8, v23
	v_mov_b32_e32 v27, v32
	v_mov_b32_e32 v143, v33
	v_pk_fma_f32 v[30:31], v[6:7], v[138:139], v[30:31]
	v_pk_add_f32 v[26:27], v[26:27], v[142:143]
.LBB0_201:
	v_cvt_pk_bf16_f32 v28, v28, v29
	v_cvt_pk_bf16_f32 v29, v24, v25
	v_mov_b64_e32 v[24:25], s[96:97]
	v_mad_i64_i32 v[22:23], s[30:31], v22, s51, v[24:25]
	v_cvt_pk_bf16_f32 v30, v30, v31
	v_cvt_pk_bf16_f32 v31, v26, v27
	v_lshl_add_u64 v[22:23], v[20:21], 1, v[22:23]
	global_store_dwordx4 v[22:23], v[28:31], off nt
	v_pk_mul_f32 v[24:25], v[136:137], s[18:19] op_sel_hi:[1,0]
	v_pk_mul_f32 v[26:27], v[132:133], s[18:19] op_sel_hi:[1,0]
	v_pk_mul_f32 v[28:29], v[134:135], s[18:19] op_sel_hi:[1,0]
	s_and_b64 vcc, exec, s[6:7]
	v_pk_mul_f32 v[30:31], v[130:131], s[18:19] op_sel_hi:[1,0]
	s_cbranch_vccnz .LBB0_203
	v_and_b32_e32 v19, 64, v195
	v_xor_b32_e32 v0, 32, v195
	v_add_u32_e32 v19, 64, v19
	v_cmp_lt_i32_e32 vcc, v0, v19
	v_pk_mul_f32 v[14:15], v[28:29], v[14:15]
	v_mul_f32_e32 v16, v24, v16
	v_cndmask_b32_e32 v0, v195, v0, vcc
	v_lshlrev_b32_e32 v0, 2, v0
	ds_bpermute_b32 v32, v0, v28
	ds_bpermute_b32 v33, v0, v29
	ds_bpermute_b32 v19, v0, v24
	ds_bpermute_b32 v130, v0, v30
	ds_bpermute_b32 v131, v0, v31
	v_mul_f32_e32 v4, v26, v4
	s_waitcnt lgkmcnt(3)
	v_pk_mul_f32 v[28:29], v[170:171], v[32:33]
	ds_bpermute_b32 v32, v0, v26
	s_waitcnt lgkmcnt(3)
	v_mul_f32_e32 v19, v170, v19
	v_mul_f32_e32 v24, v12, v19
	ds_bpermute_b32 v12, v0, v25
	ds_bpermute_b32 v0, v0, v27
	s_waitcnt lgkmcnt(2)
	v_mul_f32_e32 v19, v170, v32
	v_mul_f32_e32 v26, v8, v19
	v_mov_b32_e32 v32, v17
	s_waitcnt lgkmcnt(1)
	v_mul_f32_e32 v33, v170, v12
	v_mov_b32_e32 v12, v25
	v_pk_fma_f32 v[28:29], v[10:11], v[28:29], v[14:15]
	s_waitcnt lgkmcnt(0)
	v_mul_f32_e32 v11, v170, v0
	v_mov_b32_e32 v8, v27
	v_mov_b32_e32 v10, v5
	v_pk_mul_f32 v[12:13], v[12:13], v[32:33]
	v_pk_mul_f32 v[8:9], v[8:9], v[10:11]
	v_pk_mul_f32 v[2:3], v[30:31], v[2:3]
	v_pk_mul_f32 v[30:31], v[170:171], v[130:131]
	v_mov_b32_e32 v17, v12
	v_mov_b32_e32 v25, v13
	v_mov_b32_e32 v5, v8
	v_mov_b32_e32 v27, v9
	v_pk_add_f32 v[24:25], v[16:17], v[24:25]
	v_pk_fma_f32 v[30:31], v[6:7], v[30:31], v[2:3]
	v_pk_add_f32 v[26:27], v[4:5], v[26:27]
.LBB0_203:
	v_cvt_pk_bf16_f32 v2, v28, v29
	v_cvt_pk_bf16_f32 v3, v24, v25
	v_cvt_pk_bf16_f32 v4, v30, v31
	v_cvt_pk_bf16_f32 v5, v26, v27
	global_store_dwordx4 v[22:23], v[2:5], off offset:256 nt
	v_or_b32_e32 v22, 32, v18
	s_and_b64 vcc, exec, s[6:7]
	v_ashrrev_i32_e32 v23, 31, v22
	s_cbranch_vccnz .LBB0_205
	s_nop 1
	s_waitcnt vmcnt(8)
	v_mov_b64_e32 v[2:3], v[196:197]
	v_mov_b64_e32 v[4:5], v[198:199]
	v_mov_b64_e32 v[14:15], v[208:209]
	v_mov_b64_e32 v[16:17], v[210:211]
	v_mov_b64_e32 v[10:11], v[200:201]
	v_mov_b64_e32 v[12:13], v[202:203]
	v_mov_b64_e32 v[6:7], v[204:205]
	v_mov_b64_e32 v[8:9], v[206:207]
	v_add_u32_e32 v196, 128, v18
	v_ashrrev_i32_e32 v197, 31, v196
	v_lshlrev_b64 v[196:197], 6, v[196:197]
	v_lshl_add_u64 v[200:201], v[172:173], 0, v[196:197]
	v_lshl_add_u64 v[204:205], v[174:175], 0, v[196:197]
	global_load_dwordx4 v[196:199], v[200:201], off offset:16
	global_load_dwordx4 v[208:211], v[200:201], off
	global_load_dwordx4 v[200:203], v[204:205], off
	s_nop 0
	global_load_dwordx4 v[204:207], v[204:205], off offset:16
	s_branch .LBB0_206
.LBB0_205:
.LBB0_206:
	v_pk_mul_f32 v[24:25], v[128:129], s[18:19] op_sel_hi:[1,0]
	v_pk_mul_f32 v[28:29], v[126:127], s[18:19] op_sel_hi:[1,0]
	v_pk_mul_f32 v[26:27], v[124:125], s[18:19] op_sel_hi:[1,0]
	s_and_b64 vcc, exec, s[6:7]
	v_pk_mul_f32 v[30:31], v[122:123], s[18:19] op_sel_hi:[1,0]
	s_cbranch_vccnz .LBB0_208
	v_and_b32_e32 v19, 64, v195
	v_xor_b32_e32 v0, 32, v195
	v_add_u32_e32 v19, 64, v19
	v_cmp_lt_i32_e32 vcc, v0, v19
	v_mov_b32_e32 v130, v25
	v_mov_b32_e32 v131, v13
	v_cndmask_b32_e32 v0, v195, v0, vcc
	v_lshlrev_b32_e32 v0, 2, v0
	ds_bpermute_b32 v19, v0, v24
	ds_bpermute_b32 v32, v0, v28
	ds_bpermute_b32 v33, v0, v29
	ds_bpermute_b32 v122, v0, v30
	ds_bpermute_b32 v123, v0, v31
	s_waitcnt lgkmcnt(4)
	v_mul_f32_e32 v19, v170, v19
	v_mul_f32_e32 v124, v12, v19
	ds_bpermute_b32 v19, v0, v25
	ds_bpermute_b32 v23, v0, v26
	ds_bpermute_b32 v0, v0, v27
	v_mov_b32_e32 v128, v17
	v_pk_mul_f32 v[28:29], v[28:29], v[14:15]
	s_waitcnt lgkmcnt(2)
	v_mul_f32_e32 v129, v170, v19
	v_pk_mul_f32 v[128:129], v[130:131], v[128:129]
	v_pk_mul_f32 v[32:33], v[170:171], v[32:33]
	v_mul_f32_e32 v24, v24, v16
	v_mov_b32_e32 v25, v128
	v_mov_b32_e32 v125, v129
	v_pk_fma_f32 v[28:29], v[10:11], v[32:33], v[28:29]
	v_pk_add_f32 v[24:25], v[24:25], v[124:125]
	s_waitcnt lgkmcnt(0)
	v_mul_f32_e32 v33, v170, v0
	v_mov_b32_e32 v124, v27
	v_mov_b32_e32 v125, v9
	v_mov_b32_e32 v32, v5
	v_mul_f32_e32 v23, v170, v23
	v_pk_mul_f32 v[32:33], v[124:125], v[32:33]
	v_pk_mul_f32 v[30:31], v[30:31], v[2:3]
	v_pk_mul_f32 v[122:123], v[170:171], v[122:123]
	v_mul_f32_e32 v26, v26, v4
	v_mul_f32_e32 v126, v8, v23
	v_mov_b32_e32 v27, v32
	v_mov_b32_e32 v127, v33
	v_pk_fma_f32 v[30:31], v[6:7], v[122:123], v[30:31]
	v_pk_add_f32 v[26:27], v[26:27], v[126:127]
.LBB0_208:
	v_cvt_pk_bf16_f32 v28, v28, v29
	v_cvt_pk_bf16_f32 v29, v24, v25
	v_mov_b64_e32 v[24:25], s[96:97]
	v_mad_i64_i32 v[22:23], s[30:31], v22, s51, v[24:25]
	v_cvt_pk_bf16_f32 v30, v30, v31
	v_cvt_pk_bf16_f32 v31, v26, v27
	v_lshl_add_u64 v[22:23], v[20:21], 1, v[22:23]
	global_store_dwordx4 v[22:23], v[28:31], off nt
	v_pk_mul_f32 v[24:25], v[120:121], s[18:19] op_sel_hi:[1,0]
	v_pk_mul_f32 v[26:27], v[116:117], s[18:19] op_sel_hi:[1,0]
	v_pk_mul_f32 v[28:29], v[118:119], s[18:19] op_sel_hi:[1,0]
	s_and_b64 vcc, exec, s[6:7]
	v_pk_mul_f32 v[30:31], v[114:115], s[18:19] op_sel_hi:[1,0]
	s_cbranch_vccnz .LBB0_210
	v_and_b32_e32 v19, 64, v195
	v_xor_b32_e32 v0, 32, v195
	v_add_u32_e32 v19, 64, v19
	v_cmp_lt_i32_e32 vcc, v0, v19
	v_pk_mul_f32 v[14:15], v[28:29], v[14:15]
	v_mul_f32_e32 v16, v24, v16
	v_cndmask_b32_e32 v0, v195, v0, vcc
	v_lshlrev_b32_e32 v0, 2, v0
	ds_bpermute_b32 v32, v0, v28
	ds_bpermute_b32 v33, v0, v29
	ds_bpermute_b32 v19, v0, v24
	ds_bpermute_b32 v114, v0, v30
	ds_bpermute_b32 v115, v0, v31
	v_mul_f32_e32 v4, v26, v4
	s_waitcnt lgkmcnt(3)
	v_pk_mul_f32 v[28:29], v[170:171], v[32:33]
	ds_bpermute_b32 v32, v0, v26
	s_waitcnt lgkmcnt(3)
	v_mul_f32_e32 v19, v170, v19
	v_mul_f32_e32 v24, v12, v19
	ds_bpermute_b32 v12, v0, v25
	ds_bpermute_b32 v0, v0, v27
	s_waitcnt lgkmcnt(2)
	v_mul_f32_e32 v19, v170, v32
	v_mul_f32_e32 v26, v8, v19
	v_mov_b32_e32 v32, v17
	s_waitcnt lgkmcnt(1)
	v_mul_f32_e32 v33, v170, v12
	v_mov_b32_e32 v12, v25
	v_pk_fma_f32 v[28:29], v[10:11], v[28:29], v[14:15]
	s_waitcnt lgkmcnt(0)
	v_mul_f32_e32 v11, v170, v0
	v_mov_b32_e32 v8, v27
	v_mov_b32_e32 v10, v5
	v_pk_mul_f32 v[12:13], v[12:13], v[32:33]
	v_pk_mul_f32 v[8:9], v[8:9], v[10:11]
	v_pk_mul_f32 v[2:3], v[30:31], v[2:3]
	v_pk_mul_f32 v[30:31], v[170:171], v[114:115]
	v_mov_b32_e32 v17, v12
	v_mov_b32_e32 v25, v13
	v_mov_b32_e32 v5, v8
	v_mov_b32_e32 v27, v9
	v_pk_add_f32 v[24:25], v[16:17], v[24:25]
	v_pk_fma_f32 v[30:31], v[6:7], v[30:31], v[2:3]
	v_pk_add_f32 v[26:27], v[4:5], v[26:27]
.LBB0_210:
	v_cvt_pk_bf16_f32 v2, v28, v29
	v_cvt_pk_bf16_f32 v3, v24, v25
	v_cvt_pk_bf16_f32 v4, v30, v31
	v_cvt_pk_bf16_f32 v5, v26, v27
	global_store_dwordx4 v[22:23], v[2:5], off offset:256 nt
	v_or_b32_e32 v22, 48, v18
	s_and_b64 vcc, exec, s[6:7]
	v_ashrrev_i32_e32 v23, 31, v22
	s_cbranch_vccnz .LBB0_212
	s_nop 1
	s_waitcnt vmcnt(8)
	v_mov_b64_e32 v[2:3], v[212:213]
	v_mov_b64_e32 v[4:5], v[214:215]
	v_mov_b64_e32 v[14:15], v[224:225]
	v_mov_b64_e32 v[16:17], v[226:227]
	v_mov_b64_e32 v[10:11], v[216:217]
	v_mov_b64_e32 v[12:13], v[218:219]
	v_mov_b64_e32 v[6:7], v[220:221]
	v_mov_b64_e32 v[8:9], v[222:223]
	v_add_u32_e32 v212, 144, v18
	v_ashrrev_i32_e32 v213, 31, v212
	v_lshlrev_b64 v[212:213], 6, v[212:213]
	v_lshl_add_u64 v[216:217], v[172:173], 0, v[212:213]
	v_lshl_add_u64 v[220:221], v[174:175], 0, v[212:213]
	global_load_dwordx4 v[212:215], v[216:217], off offset:16
	global_load_dwordx4 v[224:227], v[216:217], off
	global_load_dwordx4 v[216:219], v[220:221], off
	s_nop 0
	global_load_dwordx4 v[220:223], v[220:221], off offset:16
	s_branch .LBB0_213
.LBB0_212:
.LBB0_213:
	v_pk_mul_f32 v[24:25], v[112:113], s[18:19] op_sel_hi:[1,0]
	v_pk_mul_f32 v[28:29], v[110:111], s[18:19] op_sel_hi:[1,0]
	v_pk_mul_f32 v[26:27], v[108:109], s[18:19] op_sel_hi:[1,0]
	s_and_b64 vcc, exec, s[6:7]
	v_pk_mul_f32 v[30:31], v[106:107], s[18:19] op_sel_hi:[1,0]
	s_cbranch_vccnz .LBB0_215
	v_and_b32_e32 v19, 64, v195
	v_xor_b32_e32 v0, 32, v195
	v_add_u32_e32 v19, 64, v19
	v_cmp_lt_i32_e32 vcc, v0, v19
	v_mov_b32_e32 v114, v25
	v_mov_b32_e32 v115, v13
	v_cndmask_b32_e32 v0, v195, v0, vcc
	v_lshlrev_b32_e32 v0, 2, v0
	ds_bpermute_b32 v19, v0, v24
	ds_bpermute_b32 v32, v0, v28
	ds_bpermute_b32 v33, v0, v29
	ds_bpermute_b32 v106, v0, v30
	ds_bpermute_b32 v107, v0, v31
	s_waitcnt lgkmcnt(4)
	v_mul_f32_e32 v19, v170, v19
	v_mul_f32_e32 v108, v12, v19
	ds_bpermute_b32 v19, v0, v25
	ds_bpermute_b32 v23, v0, v26
	ds_bpermute_b32 v0, v0, v27
	v_mov_b32_e32 v112, v17
	v_pk_mul_f32 v[28:29], v[28:29], v[14:15]
	s_waitcnt lgkmcnt(2)
	v_mul_f32_e32 v113, v170, v19
	v_pk_mul_f32 v[112:113], v[114:115], v[112:113]
	v_pk_mul_f32 v[32:33], v[170:171], v[32:33]
	v_mul_f32_e32 v24, v24, v16
	v_mov_b32_e32 v25, v112
	v_mov_b32_e32 v109, v113
	v_pk_fma_f32 v[28:29], v[10:11], v[32:33], v[28:29]
	v_pk_add_f32 v[24:25], v[24:25], v[108:109]
	s_waitcnt lgkmcnt(0)
	v_mul_f32_e32 v33, v170, v0
	v_mov_b32_e32 v108, v27
	v_mov_b32_e32 v109, v9
	v_mov_b32_e32 v32, v5
	v_mul_f32_e32 v23, v170, v23
	v_pk_mul_f32 v[32:33], v[108:109], v[32:33]
	v_pk_mul_f32 v[30:31], v[30:31], v[2:3]
	v_pk_mul_f32 v[106:107], v[170:171], v[106:107]
	v_mul_f32_e32 v26, v26, v4
	v_mul_f32_e32 v110, v8, v23
	v_mov_b32_e32 v27, v32
	v_mov_b32_e32 v111, v33
	v_pk_fma_f32 v[30:31], v[6:7], v[106:107], v[30:31]
	v_pk_add_f32 v[26:27], v[26:27], v[110:111]
.LBB0_215:
	v_cvt_pk_bf16_f32 v28, v28, v29
	v_cvt_pk_bf16_f32 v29, v24, v25
	v_mov_b64_e32 v[24:25], s[96:97]
	v_mad_i64_i32 v[22:23], s[30:31], v22, s51, v[24:25]
	v_cvt_pk_bf16_f32 v30, v30, v31
	v_cvt_pk_bf16_f32 v31, v26, v27
	v_lshl_add_u64 v[22:23], v[20:21], 1, v[22:23]
	global_store_dwordx4 v[22:23], v[28:31], off nt
	v_pk_mul_f32 v[24:25], v[104:105], s[18:19] op_sel_hi:[1,0]
	v_pk_mul_f32 v[26:27], v[100:101], s[18:19] op_sel_hi:[1,0]
	v_pk_mul_f32 v[28:29], v[102:103], s[18:19] op_sel_hi:[1,0]
	s_and_b64 vcc, exec, s[6:7]
	v_pk_mul_f32 v[30:31], v[98:99], s[18:19] op_sel_hi:[1,0]
	s_cbranch_vccnz .LBB0_217
	v_and_b32_e32 v19, 64, v195
	v_xor_b32_e32 v0, 32, v195
	v_add_u32_e32 v19, 64, v19
	v_cmp_lt_i32_e32 vcc, v0, v19
	v_pk_mul_f32 v[14:15], v[28:29], v[14:15]
	v_mul_f32_e32 v16, v24, v16
	v_cndmask_b32_e32 v0, v195, v0, vcc
	v_lshlrev_b32_e32 v0, 2, v0
	ds_bpermute_b32 v32, v0, v28
	ds_bpermute_b32 v33, v0, v29
	ds_bpermute_b32 v19, v0, v24
	ds_bpermute_b32 v98, v0, v30
	ds_bpermute_b32 v99, v0, v31
	v_mul_f32_e32 v4, v26, v4
	s_waitcnt lgkmcnt(3)
	v_pk_mul_f32 v[28:29], v[170:171], v[32:33]
	ds_bpermute_b32 v32, v0, v26
	s_waitcnt lgkmcnt(3)
	v_mul_f32_e32 v19, v170, v19
	v_mul_f32_e32 v24, v12, v19
	ds_bpermute_b32 v12, v0, v25
	ds_bpermute_b32 v0, v0, v27
	s_waitcnt lgkmcnt(2)
	v_mul_f32_e32 v19, v170, v32
	v_mul_f32_e32 v26, v8, v19
	v_mov_b32_e32 v32, v17
	s_waitcnt lgkmcnt(1)
	v_mul_f32_e32 v33, v170, v12
	v_mov_b32_e32 v12, v25
	v_pk_fma_f32 v[28:29], v[10:11], v[28:29], v[14:15]
	s_waitcnt lgkmcnt(0)
	v_mul_f32_e32 v11, v170, v0
	v_mov_b32_e32 v8, v27
	v_mov_b32_e32 v10, v5
	v_pk_mul_f32 v[12:13], v[12:13], v[32:33]
	v_pk_mul_f32 v[8:9], v[8:9], v[10:11]
	v_pk_mul_f32 v[2:3], v[30:31], v[2:3]
	v_pk_mul_f32 v[30:31], v[170:171], v[98:99]
	v_mov_b32_e32 v17, v12
	v_mov_b32_e32 v25, v13
	v_mov_b32_e32 v5, v8
	v_mov_b32_e32 v27, v9
	v_pk_add_f32 v[24:25], v[16:17], v[24:25]
	v_pk_fma_f32 v[30:31], v[6:7], v[30:31], v[2:3]
	v_pk_add_f32 v[26:27], v[4:5], v[26:27]
.LBB0_217:
	v_cvt_pk_bf16_f32 v2, v28, v29
	v_cvt_pk_bf16_f32 v3, v24, v25
	v_cvt_pk_bf16_f32 v4, v30, v31
	v_cvt_pk_bf16_f32 v5, v26, v27
	global_store_dwordx4 v[22:23], v[2:5], off offset:256 nt
	v_add_u32_e32 v22, 0x80, v18
	s_and_b64 vcc, exec, s[6:7]
	v_ashrrev_i32_e32 v23, 31, v22
	s_cbranch_vccnz .LBB0_219
	s_nop 1
	s_waitcnt vmcnt(8)
	v_mov_b64_e32 v[2:3], v[196:197]
	v_mov_b64_e32 v[4:5], v[198:199]
	v_mov_b64_e32 v[14:15], v[208:209]
	v_mov_b64_e32 v[16:17], v[210:211]
	v_mov_b64_e32 v[10:11], v[200:201]
	v_mov_b64_e32 v[12:13], v[202:203]
	v_mov_b64_e32 v[6:7], v[204:205]
	v_mov_b64_e32 v[8:9], v[206:207]
	v_add_u32_e32 v196, 160, v18
	v_ashrrev_i32_e32 v197, 31, v196
	v_lshlrev_b64 v[196:197], 6, v[196:197]
	v_lshl_add_u64 v[200:201], v[172:173], 0, v[196:197]
	v_lshl_add_u64 v[204:205], v[174:175], 0, v[196:197]
	global_load_dwordx4 v[196:199], v[200:201], off offset:16
	global_load_dwordx4 v[208:211], v[200:201], off
	global_load_dwordx4 v[200:203], v[204:205], off
	s_nop 0
	global_load_dwordx4 v[204:207], v[204:205], off offset:16
	s_branch .LBB0_220
.LBB0_219:
.LBB0_220:
	v_pk_mul_f32 v[24:25], v[96:97], s[18:19] op_sel_hi:[1,0]
	v_pk_mul_f32 v[28:29], v[94:95], s[18:19] op_sel_hi:[1,0]
	v_pk_mul_f32 v[26:27], v[92:93], s[18:19] op_sel_hi:[1,0]
	s_and_b64 vcc, exec, s[6:7]
	v_pk_mul_f32 v[30:31], v[90:91], s[18:19] op_sel_hi:[1,0]
	s_cbranch_vccnz .LBB0_222
	v_and_b32_e32 v19, 64, v195
	v_xor_b32_e32 v0, 32, v195
	v_add_u32_e32 v19, 64, v19
	v_cmp_lt_i32_e32 vcc, v0, v19
	v_mov_b32_e32 v98, v25
	v_mov_b32_e32 v99, v13
	v_cndmask_b32_e32 v0, v195, v0, vcc
	v_lshlrev_b32_e32 v0, 2, v0
	ds_bpermute_b32 v19, v0, v24
	ds_bpermute_b32 v32, v0, v28
	ds_bpermute_b32 v33, v0, v29
	ds_bpermute_b32 v90, v0, v30
	ds_bpermute_b32 v91, v0, v31
	s_waitcnt lgkmcnt(4)
	v_mul_f32_e32 v19, v170, v19
	v_mul_f32_e32 v92, v12, v19
	ds_bpermute_b32 v19, v0, v25
	ds_bpermute_b32 v23, v0, v26
	ds_bpermute_b32 v0, v0, v27
	v_mov_b32_e32 v96, v17
	v_pk_mul_f32 v[28:29], v[28:29], v[14:15]
	s_waitcnt lgkmcnt(2)
	v_mul_f32_e32 v97, v170, v19
	v_pk_mul_f32 v[96:97], v[98:99], v[96:97]
	v_pk_mul_f32 v[32:33], v[170:171], v[32:33]
	v_mul_f32_e32 v24, v24, v16
	v_mov_b32_e32 v25, v96
	v_mov_b32_e32 v93, v97
	v_pk_fma_f32 v[28:29], v[10:11], v[32:33], v[28:29]
	v_pk_add_f32 v[24:25], v[24:25], v[92:93]
	s_waitcnt lgkmcnt(0)
	v_mul_f32_e32 v33, v170, v0
	v_mov_b32_e32 v92, v27
	v_mov_b32_e32 v93, v9
	v_mov_b32_e32 v32, v5
	v_mul_f32_e32 v23, v170, v23
	v_pk_mul_f32 v[32:33], v[92:93], v[32:33]
	v_pk_mul_f32 v[30:31], v[30:31], v[2:3]
	v_pk_mul_f32 v[90:91], v[170:171], v[90:91]
	v_mul_f32_e32 v26, v26, v4
	v_mul_f32_e32 v94, v8, v23
	v_mov_b32_e32 v27, v32
	v_mov_b32_e32 v95, v33
	v_pk_fma_f32 v[30:31], v[6:7], v[90:91], v[30:31]
	v_pk_add_f32 v[26:27], v[26:27], v[94:95]
.LBB0_222:
	v_cvt_pk_bf16_f32 v28, v28, v29
	v_cvt_pk_bf16_f32 v29, v24, v25
	v_mov_b64_e32 v[24:25], s[96:97]
	v_mad_i64_i32 v[22:23], s[30:31], v22, s51, v[24:25]
	v_cvt_pk_bf16_f32 v30, v30, v31
	v_cvt_pk_bf16_f32 v31, v26, v27
	v_lshl_add_u64 v[22:23], v[20:21], 1, v[22:23]
	global_store_dwordx4 v[22:23], v[28:31], off nt
	v_pk_mul_f32 v[24:25], v[88:89], s[18:19] op_sel_hi:[1,0]
	v_pk_mul_f32 v[26:27], v[84:85], s[18:19] op_sel_hi:[1,0]
	v_pk_mul_f32 v[28:29], v[86:87], s[18:19] op_sel_hi:[1,0]
	s_and_b64 vcc, exec, s[6:7]
	v_pk_mul_f32 v[30:31], v[82:83], s[18:19] op_sel_hi:[1,0]
	s_cbranch_vccnz .LBB0_224
	v_and_b32_e32 v19, 64, v195
	v_xor_b32_e32 v0, 32, v195
	v_add_u32_e32 v19, 64, v19
	v_cmp_lt_i32_e32 vcc, v0, v19
	v_pk_mul_f32 v[14:15], v[28:29], v[14:15]
	v_mul_f32_e32 v16, v24, v16
	v_cndmask_b32_e32 v0, v195, v0, vcc
	v_lshlrev_b32_e32 v0, 2, v0
	ds_bpermute_b32 v32, v0, v28
	ds_bpermute_b32 v33, v0, v29
	ds_bpermute_b32 v19, v0, v24
	ds_bpermute_b32 v82, v0, v30
	ds_bpermute_b32 v83, v0, v31
	v_mul_f32_e32 v4, v26, v4
	s_waitcnt lgkmcnt(3)
	v_pk_mul_f32 v[28:29], v[170:171], v[32:33]
	ds_bpermute_b32 v32, v0, v26
	s_waitcnt lgkmcnt(3)
	v_mul_f32_e32 v19, v170, v19
	v_mul_f32_e32 v24, v12, v19
	ds_bpermute_b32 v12, v0, v25
	ds_bpermute_b32 v0, v0, v27
	s_waitcnt lgkmcnt(2)
	v_mul_f32_e32 v19, v170, v32
	v_mul_f32_e32 v26, v8, v19
	v_mov_b32_e32 v32, v17
	s_waitcnt lgkmcnt(1)
	v_mul_f32_e32 v33, v170, v12
	v_mov_b32_e32 v12, v25
	v_pk_fma_f32 v[28:29], v[10:11], v[28:29], v[14:15]
	s_waitcnt lgkmcnt(0)
	v_mul_f32_e32 v11, v170, v0
	v_mov_b32_e32 v8, v27
	v_mov_b32_e32 v10, v5
	v_pk_mul_f32 v[12:13], v[12:13], v[32:33]
	v_pk_mul_f32 v[8:9], v[8:9], v[10:11]
	v_pk_mul_f32 v[2:3], v[30:31], v[2:3]
	v_pk_mul_f32 v[30:31], v[170:171], v[82:83]
	v_mov_b32_e32 v17, v12
	v_mov_b32_e32 v25, v13
	v_mov_b32_e32 v5, v8
	v_mov_b32_e32 v27, v9
	v_pk_add_f32 v[24:25], v[16:17], v[24:25]
	v_pk_fma_f32 v[30:31], v[6:7], v[30:31], v[2:3]
	v_pk_add_f32 v[26:27], v[4:5], v[26:27]
.LBB0_224:
	v_cvt_pk_bf16_f32 v2, v28, v29
	v_cvt_pk_bf16_f32 v3, v24, v25
	v_cvt_pk_bf16_f32 v4, v30, v31
	v_cvt_pk_bf16_f32 v5, v26, v27
	global_store_dwordx4 v[22:23], v[2:5], off offset:256 nt
	v_add_u32_e32 v22, 0x90, v18
	s_and_b64 vcc, exec, s[6:7]
	v_ashrrev_i32_e32 v23, 31, v22
	s_cbranch_vccnz .LBB0_226
	s_nop 1
	s_waitcnt vmcnt(8)
	v_mov_b64_e32 v[2:3], v[212:213]
	v_mov_b64_e32 v[4:5], v[214:215]
	v_mov_b64_e32 v[14:15], v[224:225]
	v_mov_b64_e32 v[16:17], v[226:227]
	v_mov_b64_e32 v[10:11], v[216:217]
	v_mov_b64_e32 v[12:13], v[218:219]
	v_mov_b64_e32 v[6:7], v[220:221]
	v_mov_b64_e32 v[8:9], v[222:223]
	v_add_u32_e32 v212, 176, v18
	v_ashrrev_i32_e32 v213, 31, v212
	v_lshlrev_b64 v[212:213], 6, v[212:213]
	v_lshl_add_u64 v[216:217], v[172:173], 0, v[212:213]
	v_lshl_add_u64 v[220:221], v[174:175], 0, v[212:213]
	global_load_dwordx4 v[212:215], v[216:217], off offset:16
	global_load_dwordx4 v[224:227], v[216:217], off
	global_load_dwordx4 v[216:219], v[220:221], off
	s_nop 0
	global_load_dwordx4 v[220:223], v[220:221], off offset:16
	s_branch .LBB0_227
.LBB0_226:
.LBB0_227:
	v_pk_mul_f32 v[24:25], v[80:81], s[18:19] op_sel_hi:[1,0]
	v_pk_mul_f32 v[28:29], v[78:79], s[18:19] op_sel_hi:[1,0]
	v_pk_mul_f32 v[26:27], v[76:77], s[18:19] op_sel_hi:[1,0]
	s_and_b64 vcc, exec, s[6:7]
	v_pk_mul_f32 v[30:31], v[74:75], s[18:19] op_sel_hi:[1,0]
	s_cbranch_vccnz .LBB0_229
	v_and_b32_e32 v19, 64, v195
	v_xor_b32_e32 v0, 32, v195
	v_add_u32_e32 v19, 64, v19
	v_cmp_lt_i32_e32 vcc, v0, v19
	v_mov_b32_e32 v82, v25
	v_mov_b32_e32 v83, v13
	v_cndmask_b32_e32 v0, v195, v0, vcc
	v_lshlrev_b32_e32 v0, 2, v0
	ds_bpermute_b32 v19, v0, v24
	ds_bpermute_b32 v32, v0, v28
	ds_bpermute_b32 v33, v0, v29
	ds_bpermute_b32 v74, v0, v30
	ds_bpermute_b32 v75, v0, v31
	s_waitcnt lgkmcnt(4)
	v_mul_f32_e32 v19, v170, v19
	v_mul_f32_e32 v76, v12, v19
	ds_bpermute_b32 v19, v0, v25
	ds_bpermute_b32 v23, v0, v26
	ds_bpermute_b32 v0, v0, v27
	v_mov_b32_e32 v80, v17
	v_pk_mul_f32 v[28:29], v[28:29], v[14:15]
	s_waitcnt lgkmcnt(2)
	v_mul_f32_e32 v81, v170, v19
	v_pk_mul_f32 v[80:81], v[82:83], v[80:81]
	v_pk_mul_f32 v[32:33], v[170:171], v[32:33]
	v_mul_f32_e32 v24, v24, v16
	v_mov_b32_e32 v25, v80
	v_mov_b32_e32 v77, v81
	v_pk_fma_f32 v[28:29], v[10:11], v[32:33], v[28:29]
	v_pk_add_f32 v[24:25], v[24:25], v[76:77]
	s_waitcnt lgkmcnt(0)
	v_mul_f32_e32 v33, v170, v0
	v_mov_b32_e32 v76, v27
	v_mov_b32_e32 v77, v9
	v_mov_b32_e32 v32, v5
	v_mul_f32_e32 v23, v170, v23
	v_pk_mul_f32 v[32:33], v[76:77], v[32:33]
	v_pk_mul_f32 v[30:31], v[30:31], v[2:3]
	v_pk_mul_f32 v[74:75], v[170:171], v[74:75]
	v_mul_f32_e32 v26, v26, v4
	v_mul_f32_e32 v78, v8, v23
	v_mov_b32_e32 v27, v32
	v_mov_b32_e32 v79, v33
	v_pk_fma_f32 v[30:31], v[6:7], v[74:75], v[30:31]
	v_pk_add_f32 v[26:27], v[26:27], v[78:79]
.LBB0_229:
	v_cvt_pk_bf16_f32 v28, v28, v29
	v_cvt_pk_bf16_f32 v29, v24, v25
	v_mov_b64_e32 v[24:25], s[96:97]
	v_mad_i64_i32 v[22:23], s[30:31], v22, s51, v[24:25]
	v_cvt_pk_bf16_f32 v30, v30, v31
	v_cvt_pk_bf16_f32 v31, v26, v27
	v_lshl_add_u64 v[22:23], v[20:21], 1, v[22:23]
	global_store_dwordx4 v[22:23], v[28:31], off nt
	v_pk_mul_f32 v[24:25], v[72:73], s[18:19] op_sel_hi:[1,0]
	v_pk_mul_f32 v[26:27], v[68:69], s[18:19] op_sel_hi:[1,0]
	v_pk_mul_f32 v[28:29], v[70:71], s[18:19] op_sel_hi:[1,0]
	s_and_b64 vcc, exec, s[6:7]
	v_pk_mul_f32 v[30:31], v[66:67], s[18:19] op_sel_hi:[1,0]
	s_cbranch_vccnz .LBB0_231
	v_and_b32_e32 v19, 64, v195
	v_xor_b32_e32 v0, 32, v195
	v_add_u32_e32 v19, 64, v19
	v_cmp_lt_i32_e32 vcc, v0, v19
	v_pk_mul_f32 v[14:15], v[28:29], v[14:15]
	v_mul_f32_e32 v16, v24, v16
	v_cndmask_b32_e32 v0, v195, v0, vcc
	v_lshlrev_b32_e32 v0, 2, v0
	ds_bpermute_b32 v32, v0, v28
	ds_bpermute_b32 v33, v0, v29
	ds_bpermute_b32 v19, v0, v24
	ds_bpermute_b32 v66, v0, v30
	ds_bpermute_b32 v67, v0, v31
	v_mul_f32_e32 v4, v26, v4
	s_waitcnt lgkmcnt(3)
	v_pk_mul_f32 v[28:29], v[170:171], v[32:33]
	ds_bpermute_b32 v32, v0, v26
	s_waitcnt lgkmcnt(3)
	v_mul_f32_e32 v19, v170, v19
	v_mul_f32_e32 v24, v12, v19
	ds_bpermute_b32 v12, v0, v25
	ds_bpermute_b32 v0, v0, v27
	s_waitcnt lgkmcnt(2)
	v_mul_f32_e32 v19, v170, v32
	v_mul_f32_e32 v26, v8, v19
	v_mov_b32_e32 v32, v17
	s_waitcnt lgkmcnt(1)
	v_mul_f32_e32 v33, v170, v12
	v_mov_b32_e32 v12, v25
	v_pk_fma_f32 v[28:29], v[10:11], v[28:29], v[14:15]
	s_waitcnt lgkmcnt(0)
	v_mul_f32_e32 v11, v170, v0
	v_mov_b32_e32 v8, v27
	v_mov_b32_e32 v10, v5
	v_pk_mul_f32 v[12:13], v[12:13], v[32:33]
	v_pk_mul_f32 v[8:9], v[8:9], v[10:11]
	v_pk_mul_f32 v[2:3], v[30:31], v[2:3]
	v_pk_mul_f32 v[30:31], v[170:171], v[66:67]
	v_mov_b32_e32 v17, v12
	v_mov_b32_e32 v25, v13
	v_mov_b32_e32 v5, v8
	v_mov_b32_e32 v27, v9
	v_pk_add_f32 v[24:25], v[16:17], v[24:25]
	v_pk_fma_f32 v[30:31], v[6:7], v[30:31], v[2:3]
	v_pk_add_f32 v[26:27], v[4:5], v[26:27]
.LBB0_231:
	v_cvt_pk_bf16_f32 v2, v28, v29
	v_cvt_pk_bf16_f32 v3, v24, v25
	v_cvt_pk_bf16_f32 v4, v30, v31
	v_cvt_pk_bf16_f32 v5, v26, v27
	global_store_dwordx4 v[22:23], v[2:5], off offset:256 nt
	v_add_u32_e32 v22, 0xa0, v18
	s_and_b64 vcc, exec, s[6:7]
	v_ashrrev_i32_e32 v23, 31, v22
	s_cbranch_vccnz .LBB0_233
	s_nop 1
	s_waitcnt vmcnt(8)
	v_mov_b64_e32 v[2:3], v[196:197]
	v_mov_b64_e32 v[4:5], v[198:199]
	v_mov_b64_e32 v[14:15], v[208:209]
	v_mov_b64_e32 v[16:17], v[210:211]
	v_mov_b64_e32 v[10:11], v[200:201]
	v_mov_b64_e32 v[12:13], v[202:203]
	v_mov_b64_e32 v[6:7], v[204:205]
	v_mov_b64_e32 v[8:9], v[206:207]
	s_branch .LBB0_234
.LBB0_233:
.LBB0_234:
	v_pk_mul_f32 v[24:25], v[64:65], s[18:19] op_sel_hi:[1,0]
	v_pk_mul_f32 v[28:29], v[62:63], s[18:19] op_sel_hi:[1,0]
	v_pk_mul_f32 v[26:27], v[60:61], s[18:19] op_sel_hi:[1,0]
	s_and_b64 vcc, exec, s[6:7]
	v_pk_mul_f32 v[30:31], v[58:59], s[18:19] op_sel_hi:[1,0]
	s_cbranch_vccnz .LBB0_236
	v_and_b32_e32 v19, 64, v195
	v_xor_b32_e32 v0, 32, v195
	v_add_u32_e32 v19, 64, v19
	v_cmp_lt_i32_e32 vcc, v0, v19
	v_mov_b32_e32 v66, v25
	v_mov_b32_e32 v67, v13
	v_cndmask_b32_e32 v0, v195, v0, vcc
	v_lshlrev_b32_e32 v0, 2, v0
	ds_bpermute_b32 v19, v0, v24
	ds_bpermute_b32 v32, v0, v28
	ds_bpermute_b32 v33, v0, v29
	ds_bpermute_b32 v58, v0, v30
	ds_bpermute_b32 v59, v0, v31
	s_waitcnt lgkmcnt(4)
	v_mul_f32_e32 v19, v170, v19
	v_mul_f32_e32 v60, v12, v19
	ds_bpermute_b32 v19, v0, v25
	ds_bpermute_b32 v23, v0, v26
	ds_bpermute_b32 v0, v0, v27
	v_mov_b32_e32 v64, v17
	v_pk_mul_f32 v[28:29], v[28:29], v[14:15]
	s_waitcnt lgkmcnt(2)
	v_mul_f32_e32 v65, v170, v19
	v_pk_mul_f32 v[64:65], v[66:67], v[64:65]
	v_pk_mul_f32 v[32:33], v[170:171], v[32:33]
	v_mul_f32_e32 v24, v24, v16
	v_mov_b32_e32 v25, v64
	v_mov_b32_e32 v61, v65
	v_pk_fma_f32 v[28:29], v[10:11], v[32:33], v[28:29]
	v_pk_add_f32 v[24:25], v[24:25], v[60:61]
	s_waitcnt lgkmcnt(0)
	v_mul_f32_e32 v33, v170, v0
	v_mov_b32_e32 v60, v27
	v_mov_b32_e32 v61, v9
	v_mov_b32_e32 v32, v5
	v_mul_f32_e32 v23, v170, v23
	v_pk_mul_f32 v[32:33], v[60:61], v[32:33]
	v_pk_mul_f32 v[30:31], v[30:31], v[2:3]
	v_pk_mul_f32 v[58:59], v[170:171], v[58:59]
	v_mul_f32_e32 v26, v26, v4
	v_mul_f32_e32 v62, v8, v23
	v_mov_b32_e32 v27, v32
	v_mov_b32_e32 v63, v33
	v_pk_fma_f32 v[30:31], v[6:7], v[58:59], v[30:31]
	v_pk_add_f32 v[26:27], v[26:27], v[62:63]
.LBB0_236:
	v_cvt_pk_bf16_f32 v28, v28, v29
	v_cvt_pk_bf16_f32 v29, v24, v25
	v_mov_b64_e32 v[24:25], s[96:97]
	v_mad_i64_i32 v[22:23], s[30:31], v22, s51, v[24:25]
	v_cvt_pk_bf16_f32 v30, v30, v31
	v_cvt_pk_bf16_f32 v31, v26, v27
	v_lshl_add_u64 v[22:23], v[20:21], 1, v[22:23]
	global_store_dwordx4 v[22:23], v[28:31], off nt
	v_pk_mul_f32 v[24:25], v[56:57], s[18:19] op_sel_hi:[1,0]
	v_pk_mul_f32 v[26:27], v[52:53], s[18:19] op_sel_hi:[1,0]
	v_pk_mul_f32 v[28:29], v[54:55], s[18:19] op_sel_hi:[1,0]
	s_and_b64 vcc, exec, s[6:7]
	v_pk_mul_f32 v[30:31], v[50:51], s[18:19] op_sel_hi:[1,0]
	s_cbranch_vccnz .LBB0_238
	v_and_b32_e32 v19, 64, v195
	v_xor_b32_e32 v0, 32, v195
	v_add_u32_e32 v19, 64, v19
	v_cmp_lt_i32_e32 vcc, v0, v19
	v_pk_mul_f32 v[14:15], v[28:29], v[14:15]
	v_mul_f32_e32 v16, v24, v16
	v_cndmask_b32_e32 v0, v195, v0, vcc
	v_lshlrev_b32_e32 v0, 2, v0
	ds_bpermute_b32 v32, v0, v28
	ds_bpermute_b32 v33, v0, v29
	ds_bpermute_b32 v19, v0, v24
	ds_bpermute_b32 v50, v0, v30
	ds_bpermute_b32 v51, v0, v31
	v_mul_f32_e32 v4, v26, v4
	s_waitcnt lgkmcnt(3)
	v_pk_mul_f32 v[28:29], v[170:171], v[32:33]
	ds_bpermute_b32 v32, v0, v26
	s_waitcnt lgkmcnt(3)
	v_mul_f32_e32 v19, v170, v19
	v_mul_f32_e32 v24, v12, v19
	ds_bpermute_b32 v12, v0, v25
	ds_bpermute_b32 v0, v0, v27
	s_waitcnt lgkmcnt(2)
	v_mul_f32_e32 v19, v170, v32
	v_mul_f32_e32 v26, v8, v19
	v_mov_b32_e32 v32, v17
	s_waitcnt lgkmcnt(1)
	v_mul_f32_e32 v33, v170, v12
	v_mov_b32_e32 v12, v25
	v_pk_fma_f32 v[28:29], v[10:11], v[28:29], v[14:15]
	s_waitcnt lgkmcnt(0)
	v_mul_f32_e32 v11, v170, v0
	v_mov_b32_e32 v8, v27
	v_mov_b32_e32 v10, v5
	v_pk_mul_f32 v[12:13], v[12:13], v[32:33]
	v_pk_mul_f32 v[8:9], v[8:9], v[10:11]
	v_pk_mul_f32 v[2:3], v[30:31], v[2:3]
	v_pk_mul_f32 v[30:31], v[170:171], v[50:51]
	v_mov_b32_e32 v17, v12
	v_mov_b32_e32 v25, v13
	v_mov_b32_e32 v5, v8
	v_mov_b32_e32 v27, v9
	v_pk_add_f32 v[24:25], v[16:17], v[24:25]
	v_pk_fma_f32 v[30:31], v[6:7], v[30:31], v[2:3]
	v_pk_add_f32 v[26:27], v[4:5], v[26:27]
.LBB0_238:
	v_add_u32_e32 v18, 0xb0, v18
	s_and_b64 vcc, exec, s[6:7]
	v_ashrrev_i32_e32 v19, 31, v18
	v_cvt_pk_bf16_f32 v2, v28, v29
	v_cvt_pk_bf16_f32 v3, v24, v25
	v_cvt_pk_bf16_f32 v4, v30, v31
	v_cvt_pk_bf16_f32 v5, v26, v27
	global_store_dwordx4 v[22:23], v[2:5], off offset:256 nt
	s_cbranch_vccnz .LBB0_240
	s_nop 1
	s_waitcnt vmcnt(4)
	v_mov_b64_e32 v[2:3], v[212:213]
	v_mov_b64_e32 v[4:5], v[214:215]
	v_mov_b64_e32 v[14:15], v[224:225]
	v_mov_b64_e32 v[16:17], v[226:227]
	v_mov_b64_e32 v[10:11], v[216:217]
	v_mov_b64_e32 v[12:13], v[218:219]
	v_mov_b64_e32 v[6:7], v[220:221]
	v_mov_b64_e32 v[8:9], v[222:223]
	s_branch .LBB0_241

.LBB0_241:
	v_pk_mul_f32 v[22:23], v[48:49], s[18:19] op_sel_hi:[1,0]
	v_pk_mul_f32 v[26:27], v[46:47], s[18:19] op_sel_hi:[1,0]
	v_pk_mul_f32 v[24:25], v[44:45], s[18:19] op_sel_hi:[1,0]
	s_and_b64 vcc, exec, s[6:7]
	v_pk_mul_f32 v[28:29], v[42:43], s[18:19] op_sel_hi:[1,0]
	s_cbranch_vccnz .LBB0_243
	v_and_b32_e32 v19, 64, v195
	v_xor_b32_e32 v0, 32, v195
	v_add_u32_e32 v19, 64, v19
	v_cmp_lt_i32_e32 vcc, v0, v19
	v_mov_b32_e32 v48, v23
	v_mov_b32_e32 v49, v13
	v_cndmask_b32_e32 v0, v195, v0, vcc
	v_lshlrev_b32_e32 v0, 2, v0
	ds_bpermute_b32 v19, v0, v22
	ds_bpermute_b32 v43, v0, v24
	ds_bpermute_b32 v30, v0, v26
	ds_bpermute_b32 v31, v0, v27
	ds_bpermute_b32 v32, v0, v28
	s_waitcnt lgkmcnt(4)
	v_mul_f32_e32 v19, v170, v19
	v_mul_f32_e32 v42, v12, v19
	ds_bpermute_b32 v19, v0, v23
	ds_bpermute_b32 v33, v0, v29
	ds_bpermute_b32 v0, v0, v25
	v_mov_b32_e32 v46, v17
	s_waitcnt lgkmcnt(6)
	v_mul_f32_e32 v43, v170, v43
	s_waitcnt lgkmcnt(2)
	v_mul_f32_e32 v47, v170, v19
	v_pk_mul_f32 v[46:47], v[48:49], v[46:47]
	v_pk_mul_f32 v[26:27], v[26:27], v[14:15]
	v_pk_mul_f32 v[30:31], v[170:171], v[30:31]
	v_mul_f32_e32 v22, v22, v16
	v_mul_f32_e32 v44, v8, v43
	v_mov_b32_e32 v23, v46
	v_mov_b32_e32 v43, v47
	v_pk_fma_f32 v[26:27], v[10:11], v[30:31], v[26:27]
	v_pk_add_f32 v[22:23], v[22:23], v[42:43]
	s_waitcnt lgkmcnt(0)
	v_mul_f32_e32 v31, v170, v0
	v_mov_b32_e32 v42, v25
	v_mov_b32_e32 v43, v9
	v_mov_b32_e32 v30, v5
	v_pk_mul_f32 v[30:31], v[42:43], v[30:31]
	v_pk_mul_f32 v[28:29], v[28:29], v[2:3]
	v_pk_mul_f32 v[32:33], v[170:171], v[32:33]
	v_mul_f32_e32 v24, v24, v4
	v_mov_b32_e32 v25, v30
	v_mov_b32_e32 v45, v31
	v_pk_fma_f32 v[28:29], v[6:7], v[32:33], v[28:29]
	v_pk_add_f32 v[24:25], v[24:25], v[44:45]
.LBB0_243:
	v_cvt_pk_bf16_f32 v26, v26, v27
	v_cvt_pk_bf16_f32 v27, v22, v23
	v_mov_b64_e32 v[22:23], s[96:97]
	v_mad_i64_i32 v[18:19], s[30:31], v18, s51, v[22:23]
	v_lshl_add_u64 v[18:19], v[20:21], 1, v[18:19]
	v_cvt_pk_bf16_f32 v28, v28, v29
	v_cvt_pk_bf16_f32 v29, v24, v25
	global_store_dwordx4 v[18:19], v[26:29], off nt
	v_pk_mul_f32 v[20:21], v[40:41], s[18:19] op_sel_hi:[1,0]
	v_pk_mul_f32 v[24:25], v[38:39], s[18:19] op_sel_hi:[1,0]
	v_pk_mul_f32 v[22:23], v[36:37], s[18:19] op_sel_hi:[1,0]
	s_and_b64 vcc, exec, s[6:7]
	v_pk_mul_f32 v[26:27], v[34:35], s[18:19] op_sel_hi:[1,0]
	s_cbranch_vccnz .LBB0_245
	v_and_b32_e32 v28, 64, v195
	v_xor_b32_e32 v0, 32, v195
	v_add_u32_e32 v28, 64, v28
	v_cmp_lt_i32_e32 vcc, v0, v28
	v_pk_mul_f32 v[14:15], v[24:25], v[14:15]
	v_mul_f32_e32 v16, v20, v16
	v_cndmask_b32_e32 v0, v195, v0, vcc
	v_lshlrev_b32_e32 v0, 2, v0
	ds_bpermute_b32 v28, v0, v24
	ds_bpermute_b32 v29, v0, v25
	ds_bpermute_b32 v30, v0, v26
	ds_bpermute_b32 v31, v0, v27
	v_mul_f32_e32 v4, v22, v4
	v_pk_mul_f32 v[2:3], v[26:27], v[2:3]
	s_waitcnt lgkmcnt(2)
	v_pk_mul_f32 v[24:25], v[170:171], v[28:29]
	ds_bpermute_b32 v28, v0, v20
	ds_bpermute_b32 v29, v0, v22
	v_pk_fma_f32 v[24:25], v[10:11], v[24:25], v[14:15]
	v_mov_b32_e32 v10, v5
	s_waitcnt lgkmcnt(2)
	v_pk_mul_f32 v[26:27], v[170:171], v[30:31]
	s_waitcnt lgkmcnt(1)
	v_mul_f32_e32 v20, v170, v28
	v_mul_f32_e32 v20, v12, v20
	ds_bpermute_b32 v12, v0, v21
	ds_bpermute_b32 v0, v0, v23
	s_waitcnt lgkmcnt(2)
	v_mul_f32_e32 v22, v170, v29
	v_mul_f32_e32 v22, v8, v22
	v_mov_b32_e32 v28, v17
	s_waitcnt lgkmcnt(1)
	v_mul_f32_e32 v29, v170, v12
	v_mov_b32_e32 v12, v21
	s_waitcnt lgkmcnt(0)
	v_mul_f32_e32 v11, v170, v0
	v_mov_b32_e32 v8, v23
	v_pk_mul_f32 v[12:13], v[12:13], v[28:29]
	v_pk_mul_f32 v[8:9], v[8:9], v[10:11]
	v_mov_b32_e32 v17, v12
	v_mov_b32_e32 v21, v13
	v_mov_b32_e32 v5, v8
	v_mov_b32_e32 v23, v9
	v_pk_add_f32 v[20:21], v[16:17], v[20:21]
	v_pk_fma_f32 v[26:27], v[6:7], v[26:27], v[2:3]
	v_pk_add_f32 v[22:23], v[4:5], v[22:23]
